# layer-1 router RMSNorm loop: gain vector loaded once before the row loop
# speedup vs baseline: 1.0028x; 1.0028x over previous
; __global__ void __launch_bounds__(NWAVES * 64, 2) trunk_fwd(Args args) {
;     ...
;                 if (tid < 8) LC[tid] = 0;
;                 __syncthreads();
;                 const int rpb = (M + G - 1) / G, r0 = bx * rpb, r1 = (r0 + rpb) < M ? (r0 + rpb) : M;
;                 for (int m = r0 + wave; m < r1; m += NWAVES) {
;                     f32x4 v[8]; const float rstd = rms_row_load(XA + (size_t)m * D, lane, v);
;                     const f32x4* gr = (const f32x4*)gain + lane; unsigned long long* o8 = (unsigned long long*)(Hb + (size_t)m * D) + lane;
;                     float lg[8];
; #pragma unroll
;                     for (int e = 0; e < 8; ++e) lg[e] = 0.f;
; #pragma unroll
;                     for (int jj = 0; jj < 8; ++jj) { const f32x4 gg = gr[64 * jj]; const float a0 = v[jj].x * rstd * gg.x, a1 = v[jj].y * rstd * gg.y, a2 = v[jj].z * rstd * gg.z, a3 = v[jj].w * rstd * gg.w;
.LBB0_763:
	s_or_b64 exec, exec, s[0:1]
	v_cmp_gt_i32_e64 s[40:41], 8, v42
	s_and_saveexec_b64 s[0:1], s[40:41]
	v_lshl_add_u32 v2, v42, 2, 0
	v_add_u32_e32 v2, 0x10000, v2
	ds_write_b32 v2, v187
	s_or_b64 exec, exec, s[0:1]
	v_readlane_b32 s0, v253, 63
	s_add_i32 s16, s0, s22
	v_readlane_b32 s0, v253, 62
	s_cmp_ge_i32 s16, s0
	s_waitcnt vmcnt(0) lgkmcnt(0)
	s_barrier
	s_cbranch_scc1 .LBB0_774
	v_and_b32_e32 v2, 64, v228
	v_add_u32_e32 v2, 64, v2
	v_xor_b32_e32 v3, 1, v228
	v_cmp_lt_i32_e32 vcc, v3, v2
	v_lshlrev_b32_e32 v186, 4, v1
	v_lshl_add_u64 v[44:45], s[12:13], 0, v[186:187]
	v_cndmask_b32_e32 v3, v228, v3, vcc
	v_lshlrev_b32_e32 v43, 2, v3
	v_xor_b32_e32 v3, 2, v228
	v_cmp_lt_i32_e32 vcc, v3, v2
	s_mov_b64 s[0:1], 0x1000
	v_lshl_add_u64 v[46:47], v[44:45], 0, s[0:1]
	v_cndmask_b32_e32 v3, v228, v3, vcc
	v_lshlrev_b32_e32 v63, 2, v3
	v_xor_b32_e32 v3, 4, v228
	v_cmp_lt_i32_e32 vcc, v3, v2
	s_mov_b64 s[0:1], 0x1400
	v_lshl_add_u64 v[48:49], v[44:45], 0, s[0:1]
	v_cndmask_b32_e32 v3, v228, v3, vcc
	v_lshlrev_b32_e32 v65, 2, v3
	v_xor_b32_e32 v3, 8, v228
	v_cmp_lt_i32_e32 vcc, v3, v2
	s_mov_b64 s[0:1], 0x1800
	v_lshl_add_u64 v[50:51], v[44:45], 0, s[0:1]
	v_cndmask_b32_e32 v3, v228, v3, vcc
	v_lshlrev_b32_e32 v67, 2, v3
	v_xor_b32_e32 v3, 16, v228
	v_cmp_lt_i32_e32 vcc, v3, v2
	s_mov_b64 s[0:1], 0x1c00
	s_ashr_i32 s17, s16, 31
	v_cndmask_b32_e32 v3, v228, v3, vcc
	v_lshlrev_b32_e32 v69, 2, v3
	v_xor_b32_e32 v3, 32, v228
	v_lshl_add_u64 v[52:53], v[44:45], 0, s[0:1]
	s_lshl_b64 s[0:1], s[16:17], 12
	v_cmp_lt_i32_e32 vcc, v3, v2
	v_lshl_or_b32 v54, v1, 3, s0
	v_mov_b32_e32 v55, s1
	s_lshl_b64 s[0:1], s[16:17], 13
	v_cndmask_b32_e32 v2, v228, v3, vcc
	v_or_b32_e32 v56, s0, v186
	s_lshl_b32 s0, s22, 1
	v_readlane_b32 s4, v254, 21
	v_lshlrev_b32_e32 v71, 2, v2
	v_cmp_eq_u32_e64 s[42:43], 0, v1
	v_lshl_add_u32 v73, v1, 7, 0
	v_mov_b32_e32 v57, s1
	s_add_i32 s18, s4, s0
	v_readlane_b32 s5, v254, 22
	global_load_dwordx4 v[100:103], v[44:45], off
	global_load_dwordx4 v[104:107], v[44:45], off offset:1024
	global_load_dwordx4 v[108:111], v[44:45], off offset:2048
	global_load_dwordx4 v[112:115], v[44:45], off offset:3072
	global_load_dwordx4 v[116:119], v[46:47], off
	global_load_dwordx4 v[120:123], v[48:49], off
	global_load_dwordx4 v[124:127], v[50:51], off
	global_load_dwordx4 v[128:131], v[52:53], off
	s_branch .LBB0_770

; #define LAS __attribute__((address_space(3)))
; __device__ __forceinline__ unsigned pk2(float lo, float hi) { return f2bf(lo) | (f2bf(hi) << 16); }
; __global__ void __launch_bounds__(NWAVES * 64, 2) trunk_fwd(Args args) {
;     ...
;                     f32x4 v[8]; const float rstd = rms_row_load(XA + (size_t)m * D, lane, v);
;                     const f32x4* gr = (const f32x4*)gain + lane; unsigned long long* o8 = (unsigned long long*)(Hb + (size_t)m * D) + lane;
;                     float lg[8];
; #pragma unroll
;                     for (int e = 0; e < 8; ++e) lg[e] = 0.f;
; #pragma unroll
;                     for (int jj = 0; jj < 8; ++jj) { const f32x4 gg = gr[64 * jj]; const float a0 = v[jj].x * rstd * gg.x, a1 = v[jj].y * rstd * gg.y, a2 = v[jj].z * rstd * gg.z, a3 = v[jj].w * rstd * gg.w;
;                         o8[64 * jj] = (unsigned long long)pk2(a0, a1) | ((unsigned long long)pk2(a2, a3) << 32);
;                         const int c0 = 256 * jj + 4 * lane; const float av[4] = {a0, a1, a2, a3};
; #pragma unroll
;                         for (int q = 0; q < 4; ++q) { const f32x4 w0 = *(const LAS f32x4*)(RW + (c0 + q) * 8), w1 = *(const LAS f32x4*)(RW + (c0 + q) * 8 + 4);
;                             lg[0] += av[q] * w0.x; lg[1] += av[q] * w0.y; lg[2] += av[q] * w0.z; lg[3] += av[q] * w0.w; lg[4] += av[q] * w1.x; lg[5] += av[q] * w1.y; lg[6] += av[q] * w1.z; lg[7] += av[q] * w1.w; } }
.LBB0_770:
	v_readlane_b32 s4, v250, 6
	v_readlane_b32 s5, v250, 7
	s_mov_b32 s0, 0x36da2000
	s_nop 0
	v_lshl_add_u64 v[2:3], s[4:5], 0, v[56:57]
	v_add_co_u32_e32 v4, vcc, 0x36da1000, v2
	s_nop 1
	v_addc_co_u32_e32 v5, vcc, 0, v3, vcc
	global_load_dwordx4 v[30:33], v[4:5], off
	global_load_dwordx4 v[26:29], v[4:5], off offset:1024
	global_load_dwordx4 v[22:25], v[4:5], off offset:2048
	global_load_dwordx4 v[18:21], v[4:5], off offset:3072
	v_add_co_u32_e32 v2, vcc, s0, v2
	s_mov_b32 s0, 0xf800000
	s_nop 0
	v_addc_co_u32_e32 v3, vcc, 0, v3, vcc
	s_waitcnt lgkmcnt(0)
	global_load_dwordx4 v[14:17], v[2:3], off
	global_load_dwordx4 v[10:13], v[2:3], off offset:1024
	s_waitcnt vmcnt(5)
	v_mul_f32_e32 v6, v31, v31
	v_mul_f32_e32 v7, v33, v33
	v_fmac_f32_e32 v6, v30, v30
	v_fmac_f32_e32 v7, v32, v32
	v_add_f32_e32 v6, v6, v7
	s_waitcnt vmcnt(4)
	v_mul_f32_e32 v7, v27, v27
	v_mul_f32_e32 v8, v29, v29
	v_fmac_f32_e32 v7, v26, v26
	v_fmac_f32_e32 v8, v28, v28
	v_add_f32_e32 v7, v7, v8
	v_add_f32_e32 v6, v6, v7
	s_waitcnt vmcnt(3)
	v_mul_f32_e32 v7, v23, v23
	v_mul_f32_e32 v8, v25, v25
	v_fmac_f32_e32 v7, v22, v22
	v_fmac_f32_e32 v8, v24, v24
	s_waitcnt vmcnt(2)
	v_mul_f32_e32 v4, v19, v19
	v_mul_f32_e32 v5, v21, v21
	v_add_f32_e32 v7, v7, v8
	v_fmac_f32_e32 v4, v18, v18
	v_fmac_f32_e32 v5, v20, v20
	v_add_f32_e32 v6, v6, v7
	v_add_f32_e32 v4, v4, v5
	v_add_f32_e32 v4, v6, v4
	s_waitcnt vmcnt(1)
	v_mul_f32_e32 v5, v15, v15
	v_mul_f32_e32 v6, v17, v17
	v_fmac_f32_e32 v5, v14, v14
	v_fmac_f32_e32 v6, v16, v16
	v_add_f32_e32 v5, v5, v6
	v_add_f32_e32 v4, v4, v5
	s_waitcnt vmcnt(0)
	v_mul_f32_e32 v5, v11, v11
	v_mul_f32_e32 v6, v13, v13
	v_fmac_f32_e32 v5, v10, v10
	v_fmac_f32_e32 v6, v12, v12
	v_add_f32_e32 v5, v5, v6
	global_load_dwordx4 v[6:9], v[2:3], off offset:2048
	v_add_f32_e32 v4, v4, v5
	s_waitcnt vmcnt(0)
	v_mul_f32_e32 v5, v7, v7
	v_mul_f32_e32 v34, v9, v9
	v_fmac_f32_e32 v5, v6, v6
	v_fmac_f32_e32 v34, v8, v8
	v_add_f32_e32 v5, v5, v34
	v_add_f32_e32 v34, v4, v5
	global_load_dwordx4 v[2:5], v[2:3], off offset:3072
	s_waitcnt vmcnt(0)
	v_mul_f32_e32 v35, v3, v3
	v_mul_f32_e32 v36, v5, v5
	v_fmac_f32_e32 v35, v2, v2
	v_fmac_f32_e32 v36, v4, v4
	v_add_f32_e32 v35, v35, v36
	v_add_f32_e32 v34, v34, v35
	ds_bpermute_b32 v35, v43, v34
	s_waitcnt lgkmcnt(0)
	v_add_f32_e32 v34, v34, v35
	ds_bpermute_b32 v35, v63, v34
	s_waitcnt lgkmcnt(0)
	v_add_f32_e32 v34, v34, v35
	ds_bpermute_b32 v35, v65, v34
	s_waitcnt lgkmcnt(0)
	v_add_f32_e32 v34, v34, v35
	ds_bpermute_b32 v35, v67, v34
	s_waitcnt lgkmcnt(0)
	v_add_f32_e32 v34, v34, v35
	ds_bpermute_b32 v35, v69, v34
	s_waitcnt lgkmcnt(0)
	v_add_f32_e32 v34, v34, v35
	ds_bpermute_b32 v35, v71, v34
	s_waitcnt lgkmcnt(0)
	v_add_f32_e32 v34, v34, v35
	v_fmamk_f32 v34, v34, 0x3a000000, v226
	v_cmp_gt_f32_e32 vcc, s0, v34
	v_mul_f32_e32 v35, 0x4f800000, v34
	s_nop 0
	v_cndmask_b32_e32 v34, v34, v35, vcc
	v_sqrt_f32_e32 v35, v34
	s_nop 0
	v_add_u32_e32 v36, -1, v35
	v_fma_f32 v37, -v36, v35, v34
	v_cmp_ge_f32_e64 s[0:1], 0, v37
	v_add_u32_e32 v37, 1, v35
	s_nop 0
	v_cndmask_b32_e64 v36, v35, v36, s[0:1]
	v_fma_f32 v35, -v37, v35, v34
	v_cmp_lt_f32_e64 s[0:1], 0, v35
	s_nop 1
	v_cndmask_b32_e64 v35, v36, v37, s[0:1]
	v_mul_f32_e32 v36, 0x37800000, v35
	v_cndmask_b32_e32 v35, v35, v36, vcc
	v_cmp_class_f32_e32 vcc, v34, v225
	s_nop 1
	v_cndmask_b32_e32 v34, v35, v34, vcc
	v_div_scale_f32 v35, s[0:1], v34, v34, 1.0
	v_rcp_f32_e32 v36, v35
	s_mov_b32 s0, 0x34da1000
	v_fma_f32 v37, -v35, v36, 1.0
	v_fmac_f32_e32 v36, v37, v36
	v_div_scale_f32 v37, vcc, 1.0, v34, 1.0
	v_mul_f32_e32 v38, v37, v36
	v_fma_f32 v39, -v35, v38, v37
	v_fmac_f32_e32 v38, v39, v36
	v_fma_f32 v35, -v35, v38, v37
	v_div_fmas_f32 v35, v35, v36, v38
	v_div_fixup_f32 v80, v35, v34, 1.0
	v_mul_f32_e32 v30, v80, v30
	v_lshl_add_u64 v[34:35], s[4:5], 0, v[54:55]
	v_add_co_u32_e32 v58, vcc, s0, v34
	v_mul_f32_e32 v26, v80, v26
	s_nop 0
	v_addc_co_u32_e32 v59, vcc, 0, v35, vcc
	v_mul_f32_e32 v22, v80, v22
	v_mul_f32_e32 v18, v80, v18
	v_mul_f32_e32 v14, v80, v14
	v_mul_f32_e32 v10, v80, v10
	v_mul_f32_e32 v6, v80, v6
	v_mul_f32_e32 v2, v80, v2
	v_mul_f32_e32 v60, v30, v100
	v_mul_f32_e32 v30, v80, v31
	v_mul_f32_e32 v62, v30, v101
	v_mul_f32_e32 v30, v80, v32
	v_mul_f32_e32 v64, v30, v102
	v_mul_f32_e32 v30, v80, v33
	v_mul_f32_e32 v66, v30, v103
	v_bfe_u32 v30, v60, 16, 1
	v_add3_u32 v30, v60, v30, s36
	v_bfe_u32 v31, v62, 16, 1
	v_lshrrev_b32_e32 v30, 16, v30
	v_add3_u32 v31, v62, v31, s36
	v_and_or_b32 v30, v31, s27, v30
	v_bfe_u32 v31, v64, 16, 1
	v_add3_u32 v31, v64, v31, s36
	v_bfe_u32 v32, v66, 16, 1
	v_lshrrev_b32_e32 v31, 16, v31
	v_add3_u32 v32, v66, v32, s36
	v_and_or_b32 v31, v32, s27, v31
	global_store_dwordx2 v[58:59], v[30:31], off
	ds_read_b128 v[30:33], v73
	ds_read_b128 v[38:41], v73 offset:16
	ds_read_b128 v[34:37], v73 offset:32
	ds_read_b128 v[82:85], v73 offset:48
	s_waitcnt lgkmcnt(3)
	v_fma_f32 v79, v60, v32, 0
	v_fma_f32 v78, v60, v33, 0
	s_waitcnt lgkmcnt(2)
	v_fma_f32 v77, v60, v38, 0
	v_fma_f32 v76, v60, v39, 0
	v_fma_f32 v75, v60, v40, 0
	v_fma_f32 v74, v60, v41, 0
	s_waitcnt lgkmcnt(1)
	v_fmac_f32_e32 v79, v62, v36
	v_fmac_f32_e32 v78, v62, v37
	s_waitcnt lgkmcnt(0)
	v_fmac_f32_e32 v77, v62, v82
	v_fmac_f32_e32 v76, v62, v83
	v_fmac_f32_e32 v75, v62, v84
	v_fmac_f32_e32 v74, v62, v85
	ds_read_b128 v[36:39], v73 offset:64
	ds_read_b128 v[82:85], v73 offset:80
	s_waitcnt lgkmcnt(1)
	v_fmac_f32_e32 v79, v64, v38
	v_fmac_f32_e32 v78, v64, v39
	s_waitcnt lgkmcnt(0)
	v_fmac_f32_e32 v77, v64, v82
	v_fmac_f32_e32 v76, v64, v83
	v_fmac_f32_e32 v75, v64, v84
	v_fmac_f32_e32 v74, v64, v85
	ds_read_b128 v[38:41], v73 offset:96
	ds_read_b128 v[82:85], v73 offset:112
	s_waitcnt lgkmcnt(1)
; #define LAS __attribute__((address_space(3)))
; __device__ __forceinline__ unsigned pk2(float lo, float hi) { return f2bf(lo) | (f2bf(hi) << 16); }
; __global__ void __launch_bounds__(NWAVES * 64, 2) trunk_fwd(Args args) {
;     ...
; #pragma unroll
;                     for (int jj = 0; jj < 8; ++jj) { const f32x4 gg = gr[64 * jj]; const float a0 = v[jj].x * rstd * gg.x, a1 = v[jj].y * rstd * gg.y, a2 = v[jj].z * rstd * gg.z, a3 = v[jj].w * rstd * gg.w;
;                         o8[64 * jj] = (unsigned long long)pk2(a0, a1) | ((unsigned long long)pk2(a2, a3) << 32);
;                         const int c0 = 256 * jj + 4 * lane; const float av[4] = {a0, a1, a2, a3};
; #pragma unroll
;                         for (int q = 0; q < 4; ++q) { const f32x4 w0 = *(const LAS f32x4*)(RW + (c0 + q) * 8), w1 = *(const LAS f32x4*)(RW + (c0 + q) * 8 + 4);
;                             lg[0] += av[q] * w0.x; lg[1] += av[q] * w0.y; lg[2] += av[q] * w0.z; lg[3] += av[q] * w0.w; lg[4] += av[q] * w1.x; lg[5] += av[q] * w1.y; lg[6] += av[q] * w1.z; lg[7] += av[q] * w1.w; } }
	v_fmac_f32_e32 v79, v66, v40
	s_waitcnt lgkmcnt(0)
	v_fmac_f32_e32 v77, v66, v82
	v_fmac_f32_e32 v76, v66, v83
	v_fmac_f32_e32 v75, v66, v84
	v_fmac_f32_e32 v74, v66, v85
	v_fmac_f32_e32 v78, v66, v41
	v_mul_f32_e32 v72, v26, v104
	v_mul_f32_e32 v26, v80, v27
	v_mul_f32_e32 v40, v26, v105
	v_mul_f32_e32 v26, v80, v28
	v_mul_f32_e32 v68, v26, v106
	v_mul_f32_e32 v26, v80, v29
	v_mul_f32_e32 v70, v26, v107
	v_bfe_u32 v26, v72, 16, 1
	v_add3_u32 v26, v72, v26, s36
	v_bfe_u32 v27, v40, 16, 1
	v_lshrrev_b32_e32 v26, 16, v26
	v_add3_u32 v27, v40, v27, s36
	v_and_or_b32 v26, v27, s27, v26
	v_bfe_u32 v27, v68, 16, 1
	v_add3_u32 v27, v68, v27, s36
	v_bfe_u32 v28, v70, 16, 1
	v_lshrrev_b32_e32 v27, 16, v27
	v_add3_u32 v28, v70, v28, s36
	v_and_or_b32 v27, v28, s27, v27
	global_store_dwordx2 v[58:59], v[26:27], off offset:512
	v_pk_fma_f32 v[26:27], v[60:61], v[30:31], 0 op_sel_hi:[0,1,0]
	v_pk_fma_f32 v[26:27], v[62:63], v[34:35], v[26:27] op_sel_hi:[0,1,1]
	v_pk_fma_f32 v[26:27], v[64:65], v[36:37], v[26:27] op_sel_hi:[0,1,1]
	v_pk_fma_f32 v[38:39], v[66:67], v[38:39], v[26:27] op_sel_hi:[0,1,1]
	ds_read_b128 v[30:33], v73 offset:8192
	ds_read_b128 v[34:37], v73 offset:8208
	ds_read_b128 v[26:29], v73 offset:8224
	ds_read_b128 v[82:85], v73 offset:8240
	s_waitcnt lgkmcnt(3)
	v_fmac_f32_e32 v79, v72, v32
	v_fmac_f32_e32 v78, v72, v33
	v_pk_fma_f32 v[60:61], v[72:73], v[30:31], v[38:39] op_sel_hi:[0,1,1]
	s_waitcnt lgkmcnt(2)
	v_fmac_f32_e32 v77, v72, v34
	v_fmac_f32_e32 v76, v72, v35
	s_waitcnt lgkmcnt(1)
	v_fmac_f32_e32 v79, v40, v28
	v_fmac_f32_e32 v78, v40, v29
	ds_read_b128 v[28:31], v73 offset:8256
	ds_read_b128 v[32:35], v73 offset:8272
	v_fmac_f32_e32 v75, v72, v36
	v_fmac_f32_e32 v74, v72, v37
	s_waitcnt lgkmcnt(2)
	v_fmac_f32_e32 v77, v40, v82
	v_fmac_f32_e32 v76, v40, v83
	v_fmac_f32_e32 v75, v40, v84
	v_fmac_f32_e32 v74, v40, v85
	s_waitcnt lgkmcnt(1)
	v_fmac_f32_e32 v79, v68, v30
	v_fmac_f32_e32 v78, v68, v31
	s_waitcnt lgkmcnt(0)
	v_fmac_f32_e32 v77, v68, v32
	v_fmac_f32_e32 v76, v68, v33
	v_fmac_f32_e32 v75, v68, v34
	v_fmac_f32_e32 v74, v68, v35
	ds_read_b128 v[30:33], v73 offset:8288
	ds_read_b128 v[34:37], v73 offset:8304
	s_waitcnt lgkmcnt(1)
	v_fmac_f32_e32 v79, v70, v32
	v_fmac_f32_e32 v78, v70, v33
	s_waitcnt lgkmcnt(0)
	v_fmac_f32_e32 v77, v70, v34
	v_fmac_f32_e32 v76, v70, v35
	v_fmac_f32_e32 v75, v70, v36
	v_fmac_f32_e32 v74, v70, v37
	v_mul_f32_e32 v62, v22, v108
	v_mul_f32_e32 v22, v80, v23
	v_mul_f32_e32 v64, v22, v109
	v_mul_f32_e32 v22, v80, v24
	v_mul_f32_e32 v66, v22, v110
	v_mul_f32_e32 v22, v80, v25
	v_mul_f32_e32 v72, v22, v111
	v_bfe_u32 v22, v62, 16, 1
	v_add3_u32 v22, v62, v22, s36
	v_bfe_u32 v23, v64, 16, 1
	v_lshrrev_b32_e32 v22, 16, v22
	v_add3_u32 v23, v64, v23, s36
	v_and_or_b32 v22, v23, s27, v22
	v_bfe_u32 v23, v66, 16, 1
	v_add3_u32 v23, v66, v23, s36
	v_bfe_u32 v24, v72, 16, 1
	v_lshrrev_b32_e32 v23, 16, v23
	v_add3_u32 v24, v72, v24, s36
	v_and_or_b32 v23, v24, s27, v23
	global_store_dwordx2 v[58:59], v[22:23], off offset:1024
	ds_read_b128 v[22:25], v73 offset:16384
	ds_read_b128 v[36:39], v73 offset:16400
	ds_read_b128 v[32:35], v73 offset:16416
	ds_read_b128 v[82:85], v73 offset:16432
	s_waitcnt lgkmcnt(3)
	v_fmac_f32_e32 v79, v62, v24
	v_fmac_f32_e32 v78, v62, v25
	s_waitcnt lgkmcnt(2)
	v_fmac_f32_e32 v77, v62, v36
	v_fmac_f32_e32 v76, v62, v37
	v_fmac_f32_e32 v75, v62, v38
	v_fmac_f32_e32 v74, v62, v39
	s_waitcnt lgkmcnt(1)
	v_fmac_f32_e32 v79, v64, v34
	v_fmac_f32_e32 v78, v64, v35
	s_waitcnt lgkmcnt(0)
	v_fmac_f32_e32 v77, v64, v82
	v_fmac_f32_e32 v76, v64, v83
	v_fmac_f32_e32 v75, v64, v84
	v_fmac_f32_e32 v74, v64, v85
	ds_read_b128 v[34:37], v73 offset:16448
	ds_read_b128 v[82:85], v73 offset:16464
	s_waitcnt lgkmcnt(1)
	v_fmac_f32_e32 v79, v66, v36
	v_fmac_f32_e32 v78, v66, v37
	s_waitcnt lgkmcnt(0)
	v_fmac_f32_e32 v77, v66, v82
	v_fmac_f32_e32 v76, v66, v83
	v_fmac_f32_e32 v75, v66, v84
	v_fmac_f32_e32 v74, v66, v85
	ds_read_b128 v[36:39], v73 offset:16480
	ds_read_b128 v[82:85], v73 offset:16496
	s_waitcnt lgkmcnt(1)
	v_fmac_f32_e32 v79, v72, v38
	s_waitcnt lgkmcnt(0)
	v_fmac_f32_e32 v77, v72, v82
	v_fmac_f32_e32 v76, v72, v83
	v_fmac_f32_e32 v75, v72, v84
	v_fmac_f32_e32 v74, v72, v85
	v_fmac_f32_e32 v78, v72, v39
	v_mul_f32_e32 v24, v18, v112
	v_mul_f32_e32 v18, v80, v19
	v_mul_f32_e32 v38, v18, v113
	v_mul_f32_e32 v18, v80, v20
	v_mul_f32_e32 v96, v18, v114
	v_mul_f32_e32 v18, v80, v21
	v_mul_f32_e32 v98, v18, v115
	v_bfe_u32 v18, v24, 16, 1
	v_add3_u32 v18, v24, v18, s36
	v_bfe_u32 v19, v38, 16, 1
	v_lshrrev_b32_e32 v18, 16, v18
	v_add3_u32 v19, v38, v19, s36
	v_and_or_b32 v18, v19, s27, v18
	v_bfe_u32 v19, v96, 16, 1
	v_add3_u32 v19, v96, v19, s36
	v_bfe_u32 v20, v98, 16, 1
	v_lshrrev_b32_e32 v19, 16, v19
	v_add3_u32 v20, v98, v20, s36
	v_and_or_b32 v19, v20, s27, v19
	global_store_dwordx2 v[58:59], v[18:19], off offset:1536
	ds_read_b128 v[18:21], v73 offset:24576
	ds_read_b128 v[82:85], v73 offset:24592
	ds_read_b128 v[86:89], v73 offset:24608
	ds_read_b128 v[90:93], v73 offset:24624
	s_waitcnt lgkmcnt(3)
	v_fmac_f32_e32 v79, v24, v20
	v_fmac_f32_e32 v78, v24, v21
	s_waitcnt lgkmcnt(2)
	v_fmac_f32_e32 v77, v24, v82
	v_fmac_f32_e32 v76, v24, v83
	v_pk_fma_f32 v[20:21], v[40:41], v[26:27], v[60:61] op_sel_hi:[0,1,1]
	v_fmac_f32_e32 v75, v24, v84
	v_fmac_f32_e32 v74, v24, v85
	s_waitcnt lgkmcnt(1)
	v_fmac_f32_e32 v79, v38, v88
	v_fmac_f32_e32 v78, v38, v89
	s_waitcnt lgkmcnt(0)
; #define LAS __attribute__((address_space(3)))
; __device__ __forceinline__ unsigned pk2(float lo, float hi) { return f2bf(lo) | (f2bf(hi) << 16); }
; __global__ void __launch_bounds__(NWAVES * 64, 2) trunk_fwd(Args args) {
;     ...
;                     f32x4 v[8]; const float rstd = rms_row_load(XA + (size_t)m * D, lane, v);
;                     const f32x4* gr = (const f32x4*)gain + lane; unsigned long long* o8 = (unsigned long long*)(Hb + (size_t)m * D) + lane;
;                     float lg[8];
; #pragma unroll
;                     for (int e = 0; e < 8; ++e) lg[e] = 0.f;
; #pragma unroll
;                     for (int jj = 0; jj < 8; ++jj) { const f32x4 gg = gr[64 * jj]; const float a0 = v[jj].x * rstd * gg.x, a1 = v[jj].y * rstd * gg.y, a2 = v[jj].z * rstd * gg.z, a3 = v[jj].w * rstd * gg.w;
;                         o8[64 * jj] = (unsigned long long)pk2(a0, a1) | ((unsigned long long)pk2(a2, a3) << 32);
;                         const int c0 = 256 * jj + 4 * lane; const float av[4] = {a0, a1, a2, a3};
; #pragma unroll
;                         for (int q = 0; q < 4; ++q) { const f32x4 w0 = *(const LAS f32x4*)(RW + (c0 + q) * 8), w1 = *(const LAS f32x4*)(RW + (c0 + q) * 8 + 4);
;                             lg[0] += av[q] * w0.x; lg[1] += av[q] * w0.y; lg[2] += av[q] * w0.z; lg[3] += av[q] * w0.w; lg[4] += av[q] * w1.x; lg[5] += av[q] * w1.y; lg[6] += av[q] * w1.z; lg[7] += av[q] * w1.w; } }
	v_fmac_f32_e32 v77, v38, v90
	v_fmac_f32_e32 v76, v38, v91
	ds_read_b128 v[82:85], v73 offset:24640
	ds_read_b128 v[88:91], v73 offset:24656
	v_pk_fma_f32 v[20:21], v[68:69], v[28:29], v[20:21] op_sel_hi:[0,1,1]
	v_pk_fma_f32 v[20:21], v[70:71], v[30:31], v[20:21] op_sel_hi:[0,1,1]
	v_pk_fma_f32 v[20:21], v[62:63], v[22:23], v[20:21] op_sel_hi:[0,1,1]
	v_pk_fma_f32 v[20:21], v[64:65], v[32:33], v[20:21] op_sel_hi:[0,1,1]
	v_fmac_f32_e32 v75, v38, v92
	v_fmac_f32_e32 v74, v38, v93
	v_pk_fma_f32 v[20:21], v[66:67], v[34:35], v[20:21] op_sel_hi:[0,1,1]
	s_waitcnt lgkmcnt(0)
	v_fmac_f32_e32 v77, v96, v88
	v_fmac_f32_e32 v76, v96, v89
	v_fmac_f32_e32 v75, v96, v90
	v_fmac_f32_e32 v74, v96, v91
	ds_read_b128 v[88:91], v73 offset:24672
	ds_read_b128 v[92:95], v73 offset:24688
	v_pk_fma_f32 v[20:21], v[72:73], v[36:37], v[20:21] op_sel_hi:[0,1,1]
	v_pk_fma_f32 v[18:19], v[24:25], v[18:19], v[20:21] op_sel_hi:[0,1,1]
	v_pk_fma_f32 v[18:19], v[38:39], v[86:87], v[18:19] op_sel_hi:[0,1,1]
	v_pk_fma_f32 v[18:19], v[96:97], v[82:83], v[18:19] op_sel_hi:[0,1,1]
	s_waitcnt lgkmcnt(1)
	v_pk_fma_f32 v[32:33], v[98:99], v[88:89], v[18:19] op_sel_hi:[0,1,1]
	v_fmac_f32_e32 v79, v96, v84
	v_fmac_f32_e32 v78, v96, v85
	v_fmac_f32_e32 v79, v98, v90
	v_fmac_f32_e32 v78, v98, v91
	s_waitcnt lgkmcnt(0)
	v_fmac_f32_e32 v77, v98, v92
	v_fmac_f32_e32 v76, v98, v93
	v_fmac_f32_e32 v75, v98, v94
	v_fmac_f32_e32 v74, v98, v95
	v_mul_f32_e32 v34, v14, v116
	v_mul_f32_e32 v14, v80, v15
	v_mul_f32_e32 v36, v14, v117
	v_mul_f32_e32 v14, v80, v16
	v_mul_f32_e32 v38, v14, v118
	v_mul_f32_e32 v14, v80, v17
	v_mul_f32_e32 v40, v14, v119
	v_bfe_u32 v14, v34, 16, 1
	v_add3_u32 v14, v34, v14, s36
	v_bfe_u32 v15, v36, 16, 1
	v_lshrrev_b32_e32 v14, 16, v14
	v_add3_u32 v15, v36, v15, s36
	v_and_or_b32 v14, v15, s27, v14
	v_bfe_u32 v15, v38, 16, 1
	v_add3_u32 v15, v38, v15, s36
	v_bfe_u32 v16, v40, 16, 1
	v_lshrrev_b32_e32 v15, 16, v15
	v_add3_u32 v16, v40, v16, s36
	v_and_or_b32 v15, v16, s27, v15
	global_store_dwordx2 v[58:59], v[14:15], off offset:2048
	ds_read_b128 v[14:17], v73 offset:32768
	ds_read_b128 v[22:25], v73 offset:32784
	ds_read_b128 v[18:21], v73 offset:32800
	ds_read_b128 v[26:29], v73 offset:32816
	s_waitcnt lgkmcnt(3)
	v_fmac_f32_e32 v79, v34, v16
	v_fmac_f32_e32 v78, v34, v17
	s_waitcnt lgkmcnt(2)
	v_fmac_f32_e32 v77, v34, v22
	v_fmac_f32_e32 v76, v34, v23
	v_fmac_f32_e32 v75, v34, v24
	v_fmac_f32_e32 v74, v34, v25
	s_waitcnt lgkmcnt(1)
	v_fmac_f32_e32 v79, v36, v20
	v_fmac_f32_e32 v78, v36, v21
	s_waitcnt lgkmcnt(0)
	v_fmac_f32_e32 v77, v36, v26
	v_fmac_f32_e32 v76, v36, v27
	ds_read_b128 v[20:23], v73 offset:32832
	ds_read_b128 v[24:27], v73 offset:32848
	v_fmac_f32_e32 v75, v36, v28
	v_fmac_f32_e32 v74, v36, v29
	s_waitcnt lgkmcnt(1)
	v_fmac_f32_e32 v79, v38, v22
	v_fmac_f32_e32 v78, v38, v23
	s_waitcnt lgkmcnt(0)
	v_fmac_f32_e32 v77, v38, v24
	v_fmac_f32_e32 v76, v38, v25
	v_fmac_f32_e32 v75, v38, v26
	v_fmac_f32_e32 v74, v38, v27
	ds_read_b128 v[22:25], v73 offset:32864
	ds_read_b128 v[26:29], v73 offset:32880
	s_waitcnt lgkmcnt(1)
	v_fmac_f32_e32 v79, v40, v24
	v_fmac_f32_e32 v78, v40, v25
	s_waitcnt lgkmcnt(0)
	v_fmac_f32_e32 v77, v40, v26
	v_fmac_f32_e32 v76, v40, v27
	v_fmac_f32_e32 v75, v40, v28
	v_fmac_f32_e32 v74, v40, v29
	v_mul_f32_e32 v60, v10, v120
	v_mul_f32_e32 v10, v80, v11
	v_mul_f32_e32 v62, v10, v121
	v_mul_f32_e32 v10, v80, v12
	v_mul_f32_e32 v64, v10, v122
	v_mul_f32_e32 v10, v80, v13
	v_mul_f32_e32 v66, v10, v123
	v_bfe_u32 v10, v60, 16, 1
	v_add3_u32 v10, v60, v10, s36
	v_bfe_u32 v11, v62, 16, 1
	v_lshrrev_b32_e32 v10, 16, v10
	v_add3_u32 v11, v62, v11, s36
	v_and_or_b32 v10, v11, s27, v10
	v_bfe_u32 v11, v64, 16, 1
	v_add3_u32 v11, v64, v11, s36
	v_bfe_u32 v12, v66, 16, 1
	v_lshrrev_b32_e32 v11, 16, v11
	v_add3_u32 v12, v66, v12, s36
	v_and_or_b32 v11, v12, s27, v11
	global_store_dwordx2 v[58:59], v[10:11], off offset:2560
	ds_read_b128 v[10:13], v73 offset:40960
	ds_read_b128 v[28:31], v73 offset:40976
	ds_read_b128 v[24:27], v73 offset:40992
	ds_read_b128 v[82:85], v73 offset:41008
	s_waitcnt lgkmcnt(3)
	v_fmac_f32_e32 v79, v60, v12
	v_fmac_f32_e32 v78, v60, v13
	s_waitcnt lgkmcnt(2)
	v_fmac_f32_e32 v77, v60, v28
	v_fmac_f32_e32 v76, v60, v29
	v_fmac_f32_e32 v75, v60, v30
	v_fmac_f32_e32 v74, v60, v31
	s_waitcnt lgkmcnt(1)
	v_fmac_f32_e32 v79, v62, v26
	v_fmac_f32_e32 v78, v62, v27
	s_waitcnt lgkmcnt(0)
	v_fmac_f32_e32 v77, v62, v82
	v_fmac_f32_e32 v76, v62, v83
	v_fmac_f32_e32 v75, v62, v84
	v_fmac_f32_e32 v74, v62, v85
	ds_read_b128 v[26:29], v73 offset:41024
	ds_read_b128 v[82:85], v73 offset:41040
	s_waitcnt lgkmcnt(1)
	v_fmac_f32_e32 v79, v64, v28
	v_fmac_f32_e32 v78, v64, v29
	s_waitcnt lgkmcnt(0)
	v_fmac_f32_e32 v77, v64, v82
	v_fmac_f32_e32 v76, v64, v83
	v_fmac_f32_e32 v75, v64, v84
	v_fmac_f32_e32 v74, v64, v85
	ds_read_b128 v[28:31], v73 offset:41056
	ds_read_b128 v[82:85], v73 offset:41072
	s_waitcnt lgkmcnt(1)
	v_fmac_f32_e32 v79, v66, v30
	s_waitcnt lgkmcnt(0)
	v_fmac_f32_e32 v77, v66, v82
	v_fmac_f32_e32 v76, v66, v83
	v_fmac_f32_e32 v75, v66, v84
	v_fmac_f32_e32 v74, v66, v85
	v_fmac_f32_e32 v78, v66, v31
	v_mul_f32_e32 v12, v6, v124
	v_mul_f32_e32 v6, v80, v7
	v_mul_f32_e32 v7, v80, v9
	v_mul_f32_e32 v30, v6, v125
	v_mul_f32_e32 v16, v7, v127
	v_bfe_u32 v7, v12, 16, 1
	v_mul_f32_e32 v6, v80, v8
	v_add3_u32 v7, v12, v7, s36
	v_bfe_u32 v8, v30, 16, 1
	v_mul_f32_e32 v6, v6, v126
	v_lshrrev_b32_e32 v7, 16, v7
	v_add3_u32 v8, v30, v8, s36
	v_and_or_b32 v8, v8, s27, v7
	v_bfe_u32 v7, v6, 16, 1
	v_add3_u32 v7, v6, v7, s36
	v_bfe_u32 v9, v16, 16, 1
	v_lshrrev_b32_e32 v7, 16, v7
	v_add3_u32 v9, v16, v9, s36
	v_and_or_b32 v9, v9, s27, v7
	global_store_dwordx2 v[58:59], v[8:9], off offset:3072
	ds_read_b128 v[82:85], v73 offset:49152
	ds_read_b128 v[86:89], v73 offset:49168
	ds_read_b128 v[90:93], v73 offset:49184
	ds_read_b128 v[94:97], v73 offset:49200
	v_pk_fma_f32 v[8:9], v[34:35], v[14:15], v[32:33] op_sel_hi:[0,1,1]
	v_pk_fma_f32 v[8:9], v[36:37], v[18:19], v[8:9] op_sel_hi:[0,1,1]
	v_pk_fma_f32 v[8:9], v[38:39], v[20:21], v[8:9] op_sel_hi:[0,1,1]
	v_pk_fma_f32 v[8:9], v[40:41], v[22:23], v[8:9] op_sel_hi:[0,1,1]
	s_waitcnt lgkmcnt(3)
; #define LAS __attribute__((address_space(3)))
; __device__ __forceinline__ unsigned pk2(float lo, float hi) { return f2bf(lo) | (f2bf(hi) << 16); }
; __device__ __forceinline__ float wave_sum(float v) {
; #pragma unroll
;     for (int o = 1; o < 64; o <<= 1) v += __shfl_xor(v, o);
;     return v;
; __global__ void __launch_bounds__(NWAVES * 64, 2) trunk_fwd(Args args) {
;     ...
;                     for (int jj = 0; jj < 8; ++jj) { const f32x4 gg = gr[64 * jj]; const float a0 = v[jj].x * rstd * gg.x, a1 = v[jj].y * rstd * gg.y, a2 = v[jj].z * rstd * gg.z, a3 = v[jj].w * rstd * gg.w;
;                         o8[64 * jj] = (unsigned long long)pk2(a0, a1) | ((unsigned long long)pk2(a2, a3) << 32);
;                         const int c0 = 256 * jj + 4 * lane; const float av[4] = {a0, a1, a2, a3};
; #pragma unroll
;                         for (int q = 0; q < 4; ++q) { const f32x4 w0 = *(const LAS f32x4*)(RW + (c0 + q) * 8), w1 = *(const LAS f32x4*)(RW + (c0 + q) * 8 + 4);
;                             lg[0] += av[q] * w0.x; lg[1] += av[q] * w0.y; lg[2] += av[q] * w0.z; lg[3] += av[q] * w0.w; lg[4] += av[q] * w1.x; lg[5] += av[q] * w1.y; lg[6] += av[q] * w1.z; lg[7] += av[q] * w1.w; } }
; #pragma unroll
;                     for (int e = 0; e < 8; ++e) lg[e] = wave_sum(lg[e]) + args.in[I_RB][e];
;                     if (lane == 0) { int e0 = 0; float v0 = lg[0];
	v_fmac_f32_e32 v79, v12, v84
	v_fmac_f32_e32 v78, v12, v85
	s_waitcnt lgkmcnt(2)
	v_fmac_f32_e32 v77, v12, v86
	v_fmac_f32_e32 v76, v12, v87
	v_pk_fma_f32 v[8:9], v[60:61], v[10:11], v[8:9] op_sel_hi:[0,1,1]
	s_waitcnt lgkmcnt(1)
	v_fmac_f32_e32 v79, v30, v92
	v_fmac_f32_e32 v78, v30, v93
	s_waitcnt lgkmcnt(0)
	v_fmac_f32_e32 v77, v30, v94
	v_fmac_f32_e32 v76, v30, v95
	ds_read_b128 v[84:87], v73 offset:49216
	ds_read_b128 v[92:95], v73 offset:49232
	v_pk_fma_f32 v[8:9], v[62:63], v[24:25], v[8:9] op_sel_hi:[0,1,1]
	v_pk_fma_f32 v[8:9], v[64:65], v[26:27], v[8:9] op_sel_hi:[0,1,1]
	v_pk_fma_f32 v[8:9], v[66:67], v[28:29], v[8:9] op_sel_hi:[0,1,1]
	v_fmac_f32_e32 v75, v12, v88
	v_fmac_f32_e32 v74, v12, v89
	v_pk_fma_f32 v[8:9], v[12:13], v[82:83], v[8:9] op_sel_hi:[0,1,1]
	v_fmac_f32_e32 v75, v30, v96
	v_fmac_f32_e32 v74, v30, v97
	v_pk_fma_f32 v[8:9], v[30:31], v[90:91], v[8:9] op_sel_hi:[0,1,1]
	s_waitcnt lgkmcnt(1)
	v_pk_fma_f32 v[18:19], v[6:7], v[84:85], v[8:9] op_sel_hi:[0,1,1]
	v_fmac_f32_e32 v79, v6, v86
	v_fmac_f32_e32 v78, v6, v87
	s_waitcnt lgkmcnt(0)
	v_fmac_f32_e32 v77, v6, v92
	v_fmac_f32_e32 v76, v6, v93
	v_fmac_f32_e32 v75, v6, v94
	v_fmac_f32_e32 v74, v6, v95
	ds_read_b128 v[6:9], v73 offset:49248
	ds_read_b128 v[10:13], v73 offset:49264
	s_waitcnt lgkmcnt(1)
	v_fmac_f32_e32 v79, v16, v8
	v_fmac_f32_e32 v78, v16, v9
	s_waitcnt lgkmcnt(0)
	v_fmac_f32_e32 v77, v16, v10
	v_fmac_f32_e32 v76, v16, v11
	v_fmac_f32_e32 v75, v16, v12
	v_fmac_f32_e32 v74, v16, v13
	v_mul_f32_e32 v24, v2, v128
	v_mul_f32_e32 v2, v80, v3
	v_mul_f32_e32 v26, v2, v129
	v_mul_f32_e32 v2, v80, v4
	v_mul_f32_e32 v22, v2, v130
	v_mul_f32_e32 v2, v80, v5
	v_mul_f32_e32 v20, v2, v131
	v_bfe_u32 v2, v24, 16, 1
	v_add3_u32 v2, v24, v2, s36
	v_bfe_u32 v3, v26, 16, 1
	v_lshrrev_b32_e32 v2, 16, v2
	v_add3_u32 v3, v26, v3, s36
	v_and_or_b32 v2, v3, s27, v2
	v_bfe_u32 v3, v22, 16, 1
	v_add3_u32 v3, v22, v3, s36
	v_bfe_u32 v4, v20, 16, 1
	v_lshrrev_b32_e32 v3, 16, v3
	v_add3_u32 v4, v20, v4, s36
	v_and_or_b32 v3, v4, s27, v3
	global_store_dwordx2 v[58:59], v[2:3], off offset:3584
	ds_read_b128 v[8:11], v73 offset:57344
	ds_read_b128 v[12:15], v73 offset:57360
	ds_read_b128 v[2:5], v73 offset:57376
	ds_read_b128 v[28:31], v73 offset:57392
	s_waitcnt lgkmcnt(3)
	v_fmac_f32_e32 v79, v24, v10
	s_waitcnt lgkmcnt(2)
	v_fmac_f32_e32 v77, v24, v12
	v_fmac_f32_e32 v76, v24, v13
	v_fmac_f32_e32 v75, v24, v14
	v_fmac_f32_e32 v74, v24, v15
	v_fmac_f32_e32 v78, v24, v11
	s_waitcnt lgkmcnt(0)
	v_fmac_f32_e32 v77, v26, v28
	v_fmac_f32_e32 v76, v26, v29
	v_fmac_f32_e32 v75, v26, v30
	v_fmac_f32_e32 v74, v26, v31
	ds_read_b128 v[10:13], v73 offset:57408
	ds_read_b128 v[28:31], v73 offset:57424
	v_fmac_f32_e32 v79, v26, v4
	v_fmac_f32_e32 v78, v26, v5
	v_pk_fma_f32 v[4:5], v[16:17], v[6:7], v[18:19] op_sel_hi:[0,1,1]
	s_waitcnt lgkmcnt(1)
	v_fmac_f32_e32 v79, v22, v12
	v_fmac_f32_e32 v78, v22, v13
	s_waitcnt lgkmcnt(0)
	v_fmac_f32_e32 v77, v22, v28
	v_fmac_f32_e32 v76, v22, v29
	v_fmac_f32_e32 v75, v22, v30
	v_fmac_f32_e32 v74, v22, v31
	ds_read_b128 v[12:15], v73 offset:57440
	ds_read_b128 v[28:31], v73 offset:57456
	v_pk_fma_f32 v[4:5], v[24:25], v[8:9], v[4:5] op_sel_hi:[0,1,1]
	v_pk_fma_f32 v[2:3], v[26:27], v[2:3], v[4:5] op_sel_hi:[0,1,1]
	v_pk_fma_f32 v[2:3], v[22:23], v[10:11], v[2:3] op_sel_hi:[0,1,1]
	s_waitcnt lgkmcnt(1)
	v_fmac_f32_e32 v78, v20, v15
	ds_bpermute_b32 v8, v43, v78
	s_waitcnt lgkmcnt(1)
	v_fmac_f32_e32 v77, v20, v28
	v_fmac_f32_e32 v76, v20, v29
	v_pk_fma_f32 v[2:3], v[20:21], v[12:13], v[2:3] op_sel_hi:[0,1,1]
	v_fmac_f32_e32 v75, v20, v30
	s_waitcnt lgkmcnt(0)
	v_add_f32_e32 v8, v78, v8
	ds_bpermute_b32 v9, v63, v8
	v_fmac_f32_e32 v79, v20, v14
	v_fmac_f32_e32 v74, v20, v31
	ds_bpermute_b32 v4, v43, v2
	ds_bpermute_b32 v5, v43, v3
	s_waitcnt lgkmcnt(2)
	v_add_f32_e32 v8, v8, v9
	ds_bpermute_b32 v9, v65, v8
	ds_bpermute_b32 v6, v43, v79
	s_waitcnt lgkmcnt(2)
	v_pk_add_f32 v[2:3], v[2:3], v[4:5]
	ds_bpermute_b32 v4, v63, v2
	s_waitcnt lgkmcnt(2)
	v_add_f32_e32 v8, v8, v9
	ds_bpermute_b32 v9, v67, v8
	s_waitcnt lgkmcnt(2)
	v_add_f32_e32 v6, v79, v6
	ds_bpermute_b32 v5, v63, v3
	ds_bpermute_b32 v7, v63, v6
	s_waitcnt lgkmcnt(2)
	v_add_f32_e32 v8, v8, v9
	ds_bpermute_b32 v9, v69, v8
	s_waitcnt lgkmcnt(2)
	v_pk_add_f32 v[2:3], v[2:3], v[4:5]
	s_waitcnt lgkmcnt(1)
	v_add_f32_e32 v6, v6, v7
	ds_bpermute_b32 v4, v65, v2
	ds_bpermute_b32 v5, v65, v3
	s_waitcnt lgkmcnt(2)
	v_add_f32_e32 v9, v8, v9
	ds_bpermute_b32 v8, v43, v77
	ds_bpermute_b32 v7, v65, v6
	ds_bpermute_b32 v10, v71, v9
	s_waitcnt lgkmcnt(3)
	v_pk_add_f32 v[2:3], v[2:3], v[4:5]
	ds_bpermute_b32 v4, v67, v2
	s_waitcnt lgkmcnt(3)
	v_add_f32_e32 v8, v77, v8
	ds_bpermute_b32 v11, v63, v8
	s_waitcnt lgkmcnt(3)
	v_add_f32_e32 v6, v6, v7
	ds_bpermute_b32 v5, v67, v3
	ds_bpermute_b32 v7, v67, v6
	s_waitcnt lgkmcnt(2)
	v_add_f32_e32 v8, v8, v11
	ds_bpermute_b32 v11, v65, v8
	s_waitcnt lgkmcnt(2)
	v_pk_add_f32 v[2:3], v[2:3], v[4:5]
	s_waitcnt lgkmcnt(1)
	v_add_f32_e32 v6, v6, v7
	ds_bpermute_b32 v4, v69, v2
	ds_bpermute_b32 v5, v69, v3
	s_waitcnt lgkmcnt(2)
	v_add_f32_e32 v8, v8, v11
	ds_bpermute_b32 v11, v67, v8
	ds_bpermute_b32 v7, v69, v6
	s_waitcnt lgkmcnt(2)
	v_pk_add_f32 v[2:3], v[2:3], v[4:5]
	ds_bpermute_b32 v4, v71, v2
	s_waitcnt lgkmcnt(2)
	v_add_f32_e32 v8, v8, v11
	ds_bpermute_b32 v11, v69, v8
	s_waitcnt lgkmcnt(2)
	v_add_f32_e32 v6, v6, v7
	ds_bpermute_b32 v5, v71, v3
	ds_bpermute_b32 v7, v71, v6
	s_waitcnt lgkmcnt(2)
	v_add_f32_e32 v12, v8, v11
	ds_bpermute_b32 v8, v43, v76
	ds_bpermute_b32 v13, v71, v12
	s_waitcnt lgkmcnt(1)
	v_add_f32_e32 v8, v76, v8
	ds_bpermute_b32 v11, v63, v8
	s_waitcnt lgkmcnt(0)
	v_add_f32_e32 v8, v8, v11
	ds_bpermute_b32 v11, v65, v8
	s_waitcnt lgkmcnt(0)
	v_add_f32_e32 v8, v8, v11
	ds_bpermute_b32 v11, v67, v8
	s_waitcnt lgkmcnt(0)
	v_add_f32_e32 v8, v8, v11
	ds_bpermute_b32 v11, v69, v8
	s_waitcnt lgkmcnt(0)
	v_add_f32_e32 v14, v8, v11
	ds_bpermute_b32 v8, v43, v75
	ds_bpermute_b32 v15, v71, v14
	s_waitcnt lgkmcnt(1)
	v_add_f32_e32 v8, v75, v8
	ds_bpermute_b32 v11, v63, v8
	s_waitcnt lgkmcnt(0)
	v_add_f32_e32 v8, v8, v11
	ds_bpermute_b32 v11, v65, v8
	s_waitcnt lgkmcnt(0)
	v_add_f32_e32 v8, v8, v11
	ds_bpermute_b32 v11, v67, v8
	s_waitcnt lgkmcnt(0)
	v_add_f32_e32 v8, v8, v11
	ds_bpermute_b32 v11, v69, v8
	s_waitcnt lgkmcnt(0)
	v_add_f32_e32 v11, v8, v11
	ds_bpermute_b32 v8, v43, v74
	ds_bpermute_b32 v16, v71, v11
	s_waitcnt lgkmcnt(1)
	v_add_f32_e32 v8, v74, v8
	ds_bpermute_b32 v17, v63, v8
	s_waitcnt lgkmcnt(0)
	v_add_f32_e32 v8, v8, v17
	ds_bpermute_b32 v17, v65, v8
	s_waitcnt lgkmcnt(0)
	v_add_f32_e32 v8, v8, v17
	ds_bpermute_b32 v17, v67, v8
	s_waitcnt lgkmcnt(0)
	v_add_f32_e32 v8, v8, v17
	ds_bpermute_b32 v17, v69, v8
	s_waitcnt lgkmcnt(0)
	v_add_f32_e32 v8, v8, v17
	ds_bpermute_b32 v17, v71, v8
	s_and_saveexec_b64 s[20:21], s[42:43]
	s_cbranch_execz .LBB0_769
; __global__ void __launch_bounds__(NWAVES * 64, 2) trunk_fwd(Args args) {
;     ...
;                     for (int e = 0; e < 8; ++e) lg[e] = wave_sum(lg[e]) + args.in[I_RB][e];
;                     if (lane == 0) { int e0 = 0; float v0 = lg[0];
; #pragma unroll
;                         for (int e = 1; e < 8; ++e) if (lg[e] > v0) { v0 = lg[e]; e0 = e; }
;                         int e1 = -1; float v1 = -INFINITY;
; #pragma unroll
;                         for (int e = 0; e < 8; ++e) if (e != e0 && lg[e] > v1) { v1 = lg[e]; e1 = e; }
	v_readlane_b32 s44, v255, 7
	v_readlane_b32 s46, v255, 9
	v_readlane_b32 s47, v255, 10
	v_add_f32_e32 v6, v6, v7
	v_pk_add_f32 v[2:3], v[2:3], v[4:5]
	v_add_f32_e32 v9, v9, v10
	v_add_f32_e32 v12, v12, v13
	v_add_f32_e32 v14, v14, v15
	global_load_dwordx4 v[18:21], v187, s[46:47] offset:16
	global_load_dwordx4 v[22:25], v187, s[46:47]
	v_add_f32_e32 v11, v11, v16
	s_waitcnt lgkmcnt(0)
	v_add_f32_e32 v8, v8, v17
	s_mov_b32 s8, 0xff800000
	v_readlane_b32 s45, v255, 8
	v_readlane_b32 s48, v255, 11
	v_readlane_b32 s49, v255, 12
	v_readlane_b32 s50, v255, 13
	v_readlane_b32 s51, v255, 14
	s_waitcnt vmcnt(1)
	v_add_f32_e32 v12, v12, v18
	s_waitcnt vmcnt(0)
	v_add_f32_e32 v10, v6, v24
	v_pk_add_f32 v[6:7], v[2:3], v[22:23]
	v_add_f32_e32 v9, v9, v25
	v_cmp_gt_f32_e32 vcc, v7, v6
	v_add_f32_e32 v14, v14, v19
	v_add_f32_e32 v11, v11, v20
	v_cndmask_b32_e32 v2, v6, v7, vcc
	v_cndmask_b32_e64 v3, 0, 1, vcc
	v_cmp_gt_f32_e32 vcc, v10, v2
	v_add_f32_e32 v8, v8, v21
	v_cmp_nlg_f32_e64 s[8:9], s8, v6
	v_cndmask_b32_e32 v2, v2, v10, vcc
	v_cndmask_b32_e64 v3, v3, 2, vcc
	v_cmp_gt_f32_e32 vcc, v9, v2
	s_nop 1
	v_cndmask_b32_e32 v2, v2, v9, vcc
	v_cndmask_b32_e64 v3, v3, 3, vcc
	v_cmp_gt_f32_e32 vcc, v12, v2
	s_nop 1
	v_cndmask_b32_e32 v2, v2, v12, vcc
	v_cndmask_b32_e64 v3, v3, 4, vcc
	v_cmp_gt_f32_e32 vcc, v14, v2
	s_nop 1
	v_cndmask_b32_e32 v2, v2, v14, vcc
	v_cmp_ngt_f32_e64 s[0:1], v11, v2
	v_cndmask_b32_e64 v3, v3, 5, vcc
	s_nop 0
	v_cndmask_b32_e64 v4, v11, v2, s[0:1]
	v_cndmask_b32_e64 v2, 6, v3, s[0:1]
	v_cmp_gt_f32_e64 s[4:5], v8, v4
	v_cmp_ngt_f32_e32 vcc, v8, v4
	s_nop 0
	v_cndmask_b32_e64 v2, v2, 7, s[4:5]
	v_cmp_eq_u32_e64 s[6:7], 0, v2
	s_or_b64 s[6:7], s[6:7], s[8:9]
	s_or_b64 s[4:5], s[4:5], s[0:1]
	v_cndmask_b32_e64 v3, v6, v229, s[6:7]
	v_cndmask_b32_e64 v5, 0, -1, s[6:7]
	v_cmp_ne_u32_e64 s[6:7], 1, v2
	v_cmp_gt_f32_e64 s[8:9], v7, v3
	s_and_b64 s[6:7], s[6:7], s[8:9]
	v_cndmask_b32_e64 v3, v3, v7, s[6:7]
	v_cndmask_b32_e64 v5, v5, 1, s[6:7]
	v_cmp_ne_u32_e64 s[6:7], 2, v2
	v_cmp_gt_f32_e64 s[8:9], v10, v3
	s_and_b64 s[6:7], s[6:7], s[8:9]
	v_cndmask_b32_e64 v3, v3, v10, s[6:7]
	v_cndmask_b32_e64 v5, v5, 2, s[6:7]
	v_cmp_ne_u32_e64 s[6:7], 3, v2
	v_cmp_gt_f32_e64 s[8:9], v9, v3
	s_and_b64 s[6:7], s[6:7], s[8:9]
	v_cndmask_b32_e64 v3, v3, v9, s[6:7]
	v_cndmask_b32_e64 v5, v5, 3, s[6:7]
	v_cmp_ne_u32_e64 s[6:7], 4, v2
	v_cmp_gt_f32_e64 s[8:9], v12, v3
	s_and_b64 s[6:7], s[6:7], s[8:9]
	v_cndmask_b32_e64 v3, v3, v12, s[6:7]
	v_cndmask_b32_e64 v5, v5, 4, s[6:7]
	v_cmp_ne_u32_e64 s[6:7], 5, v2
	v_cmp_gt_f32_e64 s[8:9], v14, v3
	s_and_b64 s[6:7], s[6:7], s[8:9]
	v_cndmask_b32_e64 v3, v3, v14, s[6:7]
	v_cmp_gt_f32_e64 s[0:1], v11, v3
	v_cndmask_b32_e64 v6, v5, 5, s[6:7]
	s_and_b64 s[0:1], s[4:5], s[0:1]
	v_cndmask_b32_e64 v5, v3, v11, s[0:1]
	v_cndmask_b32_e64 v3, v6, 6, s[0:1]
	s_and_saveexec_b64 s[0:1], vcc
	s_cbranch_execz .LBB0_768
	v_cmp_gt_f32_e32 vcc, v8, v5
	s_and_saveexec_b64 s[4:5], vcc
	s_cbranch_execz .LBB0_767
	v_mov_b32_e32 v3, 7
	v_mov_b32_e32 v5, v8
	s_branch .LBB0_767
